# dense attention loop: MFMA/VALU re-interleaved inside each barrier segment, fp8 P fragment in fresh VGPRs, max/sum chains split
# speedup vs baseline: 1.0114x; 1.0114x over previous
.LBB0_409:
	ds_read_b128 v[200:203], v192 offset:53248
	ds_read_b128 v[68:71], v192 offset:49152
	ds_read_b128 v[72:75], v193 offset:49152
	ds_read_b128 v[204:207], v193 offset:53248
	v_add_u32_e32 v252, 0xffffe000, v152
	v_mov_b32_e32 v253, v3
	v_lshl_add_u64 v[252:253], v[148:149], 0, v[252:253]
	v_cvt_pk_fp8_f32 v232, v173, v177
	v_cvt_pk_fp8_f32 v233, v174, v178
	v_cvt_pk_fp8_f32 v234, v175, v179
	v_cvt_pk_fp8_f32 v235, v176, v180
	v_cvt_pk_fp8_f32 v232, v165, v166 op_sel:[0,0,1]
	v_cvt_pk_fp8_f32 v233, v167, v168 op_sel:[0,0,1]
	v_cvt_pk_fp8_f32 v234, v169, v170 op_sel:[0,0,1]
	s_waitcnt lgkmcnt(1)
	v_mfma_scale_f32_32x32x64_f8f6f4 v[84:99], v[68:75], v[100:107], 0, v188, v188 op_sel_hi:[0,0,0]
	v_cvt_pk_fp8_f32 v235, v171, v172 op_sel:[0,0,1]
	v_exp_f32_e32 v154, v154
	v_add_f32_e32 v240, v173, v177
	v_exp_f32_e32 v155, v155
	v_add_f32_e32 v240, v165, v240
	v_exp_f32_e32 v130, v130
	v_add_f32_e32 v240, v166, v240
	v_exp_f32_e32 v131, v131
	v_add_f32_e32 v240, v174, v240
	v_exp_f32_e32 v128, v128
	s_waitcnt lgkmcnt(0)
	v_mfma_scale_f32_32x32x64_f8f6f4 v[68:83], v[200:207], v[100:107], 0, v188, v188 op_sel_hi:[0,0,0]
	ds_read_b128 v[200:203], v194 offset:53248
	ds_read_b128 v[208:211], v194 offset:49152
	ds_read_b128 v[212:215], v195 offset:49152
	ds_read_b128 v[204:207], v195 offset:53248
	v_add_f32_e32 v240, v178, v240
	v_exp_f32_e32 v129, v129
	v_add_f32_e32 v240, v167, v240
	v_exp_f32_e32 v126, v126
	v_add_f32_e32 v240, v168, v240
	v_exp_f32_e32 v127, v127
	v_add_f32_e32 v240, v175, v240
	v_exp_f32_e32 v124, v124
	v_add_f32_e32 v240, v179, v240
	v_exp_f32_e32 v125, v125
	v_add_f32_e32 v240, v169, v240
	s_waitcnt lgkmcnt(1)
	v_mfma_scale_f32_32x32x64_f8f6f4 v[84:99], v[208:215], v[108:115], v[84:99], v188, v188 op_sel_hi:[0,0,0]
	v_exp_f32_e32 v160, v160
	v_add_f32_e32 v240, v170, v240
	v_exp_f32_e32 v161, v161
	v_add_f32_e32 v240, v176, v240
	v_exp_f32_e32 v158, v158
	v_add_f32_e32 v240, v180, v240
	v_exp_f32_e32 v159, v159
	v_add_f32_e32 v240, v171, v240
	v_exp_f32_e32 v156, v156
	v_add_f32_e32 v240, v172, v240
	v_exp_f32_e32 v157, v157
	s_waitcnt lgkmcnt(0)
	v_mfma_scale_f32_32x32x64_f8f6f4 v[68:83], v[200:207], v[108:115], v[68:83], v188, v188 op_sel_hi:[0,0,0]
	ds_read_b128 v[164:167], v197
	ds_read_b128 v[172:175], v197 offset:2048
	ds_read_b128 v[168:171], v198
	ds_read_b128 v[176:179], v198 offset:2048
	ds_read_b128 v[200:203], v197 offset:4096
	ds_read_b128 v[208:211], v197 offset:6144
	ds_read_b128 v[204:207], v198 offset:4096
	ds_read_b128 v[212:215], v198 offset:6144
	v_cvt_pk_fp8_f32 v236, v154, v155
	v_cvt_pk_fp8_f32 v237, v128, v129
	v_cvt_pk_fp8_f32 v238, v124, v125
	v_cvt_pk_fp8_f32 v239, v158, v159
	v_cvt_pk_fp8_f32 v236, v130, v131 op_sel:[0,0,1]
	v_cvt_pk_fp8_f32 v237, v126, v127 op_sel:[0,0,1]
	v_cvt_pk_fp8_f32 v238, v160, v161 op_sel:[0,0,1]
	v_cvt_pk_fp8_f32 v239, v156, v157 op_sel:[0,0,1]
	v_add_f32_e32 v241, v128, v129
	v_add_f32_e32 v241, v124, v241
	v_add_f32_e32 v241, v125, v241
	v_add_f32_e32 v241, v126, v241
	v_add_f32_e32 v241, v127, v241
	global_load_dwordx4 v[124:127], v[150:151], off offset:-64
	v_add_f32_e32 v241, v130, v241
	v_add_f32_e32 v241, v131, v241
	global_load_dwordx4 v[128:131], v[252:253], off
	s_waitcnt lgkmcnt(5)
	v_mfma_scale_f32_32x32x64_f8f6f4 v[52:67], v[232:239], v[164:171], v[52:67], v188, v188 op_sel_hi:[0,0,0]
	v_add_f32_e32 v241, v154, v241
	v_add_f32_e32 v241, v155, v241
	v_add_f32_e32 v241, v160, v241
	v_add_f32_e32 v241, v161, v241
	v_add_f32_e32 v241, v158, v241
	v_add_f32_e32 v241, v159, v241
	v_add_f32_e32 v241, v156, v241
	v_add_f32_e32 v241, v157, v241
	v_add_f32_e32 v162, v240, v241
	v_mov_b32_e32 v163, v162
	s_waitcnt lgkmcnt(4)
	v_mfma_scale_f32_32x32x64_f8f6f4 v[36:51], v[232:239], v[172:179], v[36:51], v188, v188 op_sel_hi:[0,0,0]
	v_permlane32_swap_b32_e32 v162, v163
	v_max3_f32 v246, v84, v85, v86
	v_max3_f32 v246, v246, v87, v88
	v_max3_f32 v246, v246, v89, v90
	v_max3_f32 v246, v246, v91, v92
	v_max3_f32 v246, v246, v93, v94
	v_max3_f32 v246, v246, v95, v96
	v_max3_f32 v246, v246, v97, v98
	v_max_f32_e32 v246, v246, v99
	v_max3_f32 v248, v68, v69, v70
	s_waitcnt lgkmcnt(1)
	v_mfma_scale_f32_32x32x64_f8f6f4 v[20:35], v[232:239], v[200:207], v[20:35], v188, v188 op_sel_hi:[0,0,0]
	v_max3_f32 v248, v248, v71, v72
	v_max3_f32 v248, v248, v73, v74
	v_max3_f32 v248, v248, v75, v76
	v_max3_f32 v248, v248, v77, v78
	v_max3_f32 v248, v248, v79, v80
	v_max3_f32 v248, v248, v81, v82
	v_max_f32_e32 v248, v248, v83
	v_max_f32_e32 v250, v246, v248
	v_mov_b32_e32 v251, v250
	s_nop 0
	s_nop 0
	v_permlane32_swap_b32_e32 v250, v251
	s_waitcnt lgkmcnt(0)
	v_mfma_scale_f32_32x32x64_f8f6f4 v[4:19], v[232:239], v[208:215], v[4:19], v188, v188 op_sel_hi:[0,0,0]
	v_max_f32_e32 v250, v250, v251
	v_sub_f32_e32 v154, v250, v153
	v_max_f32_e32 v2, v153, v250
	v_sub_f32_e32 v155, v153, v2
	v_mul_f32_e32 v155, 0x3e0293ee, v155
	v_exp_f32_e32 v155, v155
	v_cmp_ge_f32_e32 vcc, s55, v154
	s_cmp_eq_u64 vcc, exec
	s_cselect_b64 s[4:5], -1, 0
	s_barrier
	s_waitcnt vmcnt(2)
	v_cndmask_b32_e64 v164, v155, 1.0, s[4:5]
	s_waitcnt vmcnt(2)
	v_mov_b32_e32 v154, v116
	v_mov_b32_e32 v155, v118
	ds_write_b64 v189, v[154:155]
	v_mov_b32_e32 v154, v117
	v_mov_b32_e32 v155, v119
	v_cmp_gt_f32_e32 vcc, 1.0, v164
	ds_write_b64 v190, v[154:155]
	ds_write_b128 v191, v[120:123] offset:32768
	s_cbranch_vccz .LBB0_413
	s_and_saveexec_b64 s[8:9], s[6:7]
	ds_write_b32 v184, v164 offset:128
	s_or_b64 exec, exec, s[8:9]
	s_waitcnt lgkmcnt(0)
	v_add_u32_e32 v165, v135, v185
	ds_read_b128 v[154:157], v165 offset:224
	ds_read_b128 v[158:161], v165 offset:192
	ds_read_b128 v[166:169], v165 offset:160
	ds_read_b128 v[170:173], v165 offset:128
	s_waitcnt lgkmcnt(3)
	v_pk_mul_f32 v[64:65], v[64:65], v[154:155]
	s_waitcnt lgkmcnt(2)
	v_pk_mul_f32 v[60:61], v[60:61], v[158:159]
	s_waitcnt lgkmcnt(1)
	v_pk_mul_f32 v[56:57], v[56:57], v[166:167]
	v_pk_mul_f32 v[66:67], v[66:67], v[156:157]
	v_pk_mul_f32 v[62:63], v[62:63], v[160:161]
	v_pk_mul_f32 v[58:59], v[58:59], v[168:169]
	s_waitcnt lgkmcnt(0)
	v_pk_mul_f32 v[54:55], v[54:55], v[172:173]
	v_pk_mul_f32 v[52:53], v[52:53], v[170:171]
	v_pk_mul_f32 v[48:49], v[48:49], v[154:155]
	v_pk_mul_f32 v[44:45], v[44:45], v[158:159]
	v_pk_mul_f32 v[40:41], v[40:41], v[166:167]
	v_pk_mul_f32 v[50:51], v[50:51], v[156:157]
	v_pk_mul_f32 v[46:47], v[46:47], v[160:161]
	v_pk_mul_f32 v[42:43], v[42:43], v[168:169]
	v_pk_mul_f32 v[38:39], v[38:39], v[172:173]
	v_pk_mul_f32 v[36:37], v[36:37], v[170:171]
	v_pk_mul_f32 v[32:33], v[32:33], v[154:155]
	v_pk_mul_f32 v[28:29], v[28:29], v[158:159]
	v_pk_mul_f32 v[24:25], v[24:25], v[166:167]
	v_pk_mul_f32 v[34:35], v[34:35], v[156:157]
	v_pk_mul_f32 v[30:31], v[30:31], v[160:161]
	v_pk_mul_f32 v[26:27], v[26:27], v[168:169]
	v_pk_mul_f32 v[22:23], v[22:23], v[172:173]
	v_pk_mul_f32 v[20:21], v[20:21], v[170:171]
	v_pk_mul_f32 v[16:17], v[16:17], v[154:155]
	v_pk_mul_f32 v[12:13], v[12:13], v[158:159]
	v_pk_mul_f32 v[8:9], v[8:9], v[166:167]
	v_pk_mul_f32 v[18:19], v[18:19], v[156:157]
	v_pk_mul_f32 v[14:15], v[14:15], v[160:161]
	v_pk_mul_f32 v[10:11], v[10:11], v[168:169]
	v_pk_mul_f32 v[6:7], v[6:7], v[172:173]
	v_pk_mul_f32 v[4:5], v[4:5], v[170:171]
.LBB0_413:
	v_cndmask_b32_e64 v154, v2, v153, s[4:5]
	v_mul_f32_e32 v153, 0xbe0293ee, v154
	v_fmamk_f32 v2, v84, 0x3e0293ee, v153
	v_fmamk_f32 v84, v85, 0x3e0293ee, v153
	v_fmamk_f32 v85, v86, 0x3e0293ee, v153
	v_fmamk_f32 v86, v87, 0x3e0293ee, v153
	v_fmamk_f32 v87, v88, 0x3e0293ee, v153
	v_fmamk_f32 v88, v89, 0x3e0293ee, v153
	v_fmamk_f32 v89, v90, 0x3e0293ee, v153
	v_fmamk_f32 v90, v91, 0x3e0293ee, v153
	v_fmamk_f32 v91, v92, 0x3e0293ee, v153
	v_fmamk_f32 v92, v93, 0x3e0293ee, v153
	v_fmamk_f32 v93, v94, 0x3e0293ee, v153
	v_fmamk_f32 v94, v95, 0x3e0293ee, v153
	v_fmamk_f32 v95, v96, 0x3e0293ee, v153
	v_fmamk_f32 v96, v97, 0x3e0293ee, v153
	v_fmamk_f32 v97, v98, 0x3e0293ee, v153
	v_fmamk_f32 v98, v99, 0x3e0293ee, v153
	v_exp_f32_e32 v165, v2
	v_exp_f32_e32 v169, v84
	v_exp_f32_e32 v2, v85
	v_exp_f32_e32 v155, v86
	v_exp_f32_e32 v166, v87
	v_exp_f32_e32 v170, v88
	v_exp_f32_e32 v156, v89
	v_exp_f32_e32 v157, v90
	v_exp_f32_e32 v167, v91
	v_exp_f32_e32 v171, v92
	v_exp_f32_e32 v158, v93
	v_exp_f32_e32 v159, v94
	v_exp_f32_e32 v168, v95
	v_exp_f32_e32 v172, v96
	v_exp_f32_e32 v160, v97
	v_exp_f32_e32 v161, v98
	v_fmamk_f32 v173, v68, 0x3e0293ee, v153
	v_fmamk_f32 v174, v69, 0x3e0293ee, v153
	v_fmamk_f32 v175, v70, 0x3e0293ee, v153
	v_fmamk_f32 v176, v71, 0x3e0293ee, v153
	v_fmamk_f32 v177, v72, 0x3e0293ee, v153
	v_fmamk_f32 v178, v73, 0x3e0293ee, v153
	v_fmamk_f32 v179, v74, 0x3e0293ee, v153
	v_fmamk_f32 v180, v75, 0x3e0293ee, v153
	v_fmamk_f32 v181, v76, 0x3e0293ee, v153
	v_fmamk_f32 v182, v77, 0x3e0293ee, v153
	v_fmamk_f32 v183, v78, 0x3e0293ee, v153
	v_fmamk_f32 v200, v79, 0x3e0293ee, v153
	v_fmamk_f32 v201, v80, 0x3e0293ee, v153
	v_fmamk_f32 v208, v81, 0x3e0293ee, v153
	v_fmamk_f32 v209, v82, 0x3e0293ee, v153
	v_fmac_f32_e32 v153, 0x3e0293ee, v83
	s_waitcnt lgkmcnt(0)
	s_barrier
	s_cmp_gt_u32 s15, 60
	s_cselect_b64 s[8:9], -1, 0
	s_and_b64 vcc, exec, s[8:9]
	s_cbranch_vccnz .Lattnb_noload
	v_mov_b32_e32 v244, v152
	v_mov_b32_e32 v245, v3
	v_lshl_add_u64 v[120:121], v[148:149], 0, v[244:245]
	global_load_dwordx4 v[116:119], v[150:151], off
	s_nop 0
	global_load_dwordx4 v[120:123], v[120:121], off
.Lattnb_noload:
	ds_read_b128 v[210:213], v192 offset:36864
	ds_read_b128 v[68:71], v192 offset:32768
	ds_read_b128 v[72:75], v193 offset:32768
	ds_read_b128 v[214:217], v193 offset:36864
	v_cvt_pk_fp8_f32 v232, v165, v169
	v_cvt_pk_fp8_f32 v233, v166, v170
	v_cvt_pk_fp8_f32 v234, v167, v171
	v_cvt_pk_fp8_f32 v235, v168, v172
	v_cvt_pk_fp8_f32 v232, v2, v155 op_sel:[0,0,1]
	v_cvt_pk_fp8_f32 v233, v156, v157 op_sel:[0,0,1]
	v_cvt_pk_fp8_f32 v234, v158, v159 op_sel:[0,0,1]
	v_cvt_pk_fp8_f32 v235, v160, v161 op_sel:[0,0,1]
	v_exp_f32_e32 v173, v173
	v_add_f32_e32 v240, v165, v169
	s_waitcnt lgkmcnt(1)
	v_mfma_scale_f32_32x32x64_f8f6f4 v[84:99], v[68:75], v[100:107], 0, v188, v188 op_sel_hi:[0,0,0]
	v_exp_f32_e32 v174, v174
	v_add_f32_e32 v240, v2, v240
	v_exp_f32_e32 v175, v175
	v_add_f32_e32 v240, v155, v240
	v_exp_f32_e32 v176, v176
	v_add_f32_e32 v240, v166, v240
	v_exp_f32_e32 v177, v177
	v_add_f32_e32 v240, v170, v240
	v_exp_f32_e32 v178, v178
	v_add_f32_e32 v240, v156, v240
	s_waitcnt lgkmcnt(0)
	v_mfma_scale_f32_32x32x64_f8f6f4 v[68:83], v[210:217], v[100:107], 0, v188, v188 op_sel_hi:[0,0,0]
	ds_read_b128 v[210:213], v194 offset:36864
	ds_read_b128 v[218:221], v194 offset:32768
	ds_read_b128 v[222:225], v195 offset:32768
	ds_read_b128 v[214:217], v195 offset:36864
	v_exp_f32_e32 v179, v179
	v_add_f32_e32 v240, v157, v240
	v_exp_f32_e32 v180, v180
	v_add_f32_e32 v240, v167, v240
	v_exp_f32_e32 v181, v181
	v_add_f32_e32 v240, v171, v240
	v_exp_f32_e32 v182, v182
	v_add_f32_e32 v240, v158, v240
	v_exp_f32_e32 v183, v183
	v_add_f32_e32 v240, v159, v240
	s_waitcnt lgkmcnt(1)
	v_mfma_scale_f32_32x32x64_f8f6f4 v[84:99], v[218:225], v[108:115], v[84:99], v188, v188 op_sel_hi:[0,0,0]
	v_exp_f32_e32 v200, v200
	v_add_f32_e32 v240, v168, v240
	v_exp_f32_e32 v201, v201
	v_add_f32_e32 v240, v172, v240
	v_exp_f32_e32 v208, v208
	v_add_f32_e32 v240, v160, v240
	v_exp_f32_e32 v209, v209
	v_add_f32_e32 v240, v161, v240
	v_exp_f32_e32 v153, v153
	v_cvt_pk_fp8_f32 v236, v173, v174
	s_waitcnt lgkmcnt(0)
	v_mfma_scale_f32_32x32x64_f8f6f4 v[68:83], v[210:217], v[108:115], v[68:83], v188, v188 op_sel_hi:[0,0,0]
	ds_read_b128 v[166:169], v197 offset:16384
	v_cvt_pk_fp8_f32 v237, v177, v178
	v_cvt_pk_fp8_f32 v238, v181, v182
	v_cvt_pk_fp8_f32 v239, v201, v208
	v_cvt_pk_fp8_f32 v236, v175, v176 op_sel:[0,0,1]
	v_cvt_pk_fp8_f32 v237, v179, v180 op_sel:[0,0,1]
	v_cvt_pk_fp8_f32 v238, v183, v200 op_sel:[0,0,1]
	v_cvt_pk_fp8_f32 v239, v209, v153 op_sel:[0,0,1]
	v_add_f32_e32 v241, v173, v200
	v_add_f32_e32 v241, v201, v241
	ds_read_b128 v[200:203], v197 offset:18432
	ds_read_b128 v[170:173], v198 offset:16384
	ds_read_b128 v[204:207], v198 offset:18432
	ds_read_b128 v[216:219], v197 offset:20480
	ds_read_b128 v[224:227], v197 offset:22528
	ds_read_b128 v[220:223], v198 offset:20480
	ds_read_b128 v[228:231], v198 offset:22528
	v_add_f32_e32 v241, v174, v241
	s_waitcnt lgkmcnt(5)
	v_mfma_scale_f32_32x32x64_f8f6f4 v[52:67], v[232:239], v[166:173], v[52:67], v188, v188 op_sel_hi:[0,0,0]
	v_add_f32_e32 v241, v175, v241
	v_add_f32_e32 v241, v176, v241
	v_add_f32_e32 v241, v177, v241
	v_add_f32_e32 v241, v178, v241
	v_add_f32_e32 v241, v179, v241
	v_add_f32_e32 v241, v180, v241
	v_add_f32_e32 v241, v181, v241
	v_add_f32_e32 v241, v182, v241
	v_add_f32_e32 v241, v183, v241
	v_add_f32_e32 v241, v208, v241
	v_add_f32_e32 v241, v209, v241
	s_waitcnt lgkmcnt(4)
	v_mfma_scale_f32_32x32x64_f8f6f4 v[36:51], v[232:239], v[200:207], v[36:51], v188, v188 op_sel_hi:[0,0,0]
	v_add_f32_e32 v241, v153, v241
	v_add_f32_e32 v181, v240, v241
	v_mov_b32_e32 v182, v181
	s_nop 0
	s_nop 0
	v_permlane32_swap_b32_e32 v181, v182
	v_max3_f32 v246, v84, v85, v86
	v_max3_f32 v246, v246, v87, v88
	v_max3_f32 v246, v246, v89, v90
	v_max3_f32 v246, v246, v91, v92
	v_max3_f32 v246, v246, v93, v94
	v_max3_f32 v246, v246, v95, v96
	v_max3_f32 v246, v246, v97, v98
	s_waitcnt lgkmcnt(1)
	v_mfma_scale_f32_32x32x64_f8f6f4 v[20:35], v[232:239], v[216:223], v[20:35], v188, v188 op_sel_hi:[0,0,0]
	v_max_f32_e32 v246, v246, v99
	v_max3_f32 v248, v68, v69, v70
	v_max3_f32 v248, v248, v71, v72
	v_max3_f32 v248, v248, v73, v74
	v_max3_f32 v248, v248, v75, v76
	v_max3_f32 v248, v248, v77, v78
	v_max3_f32 v248, v248, v79, v80
	v_max3_f32 v248, v248, v81, v82
	v_max_f32_e32 v248, v248, v83
	v_max_f32_e32 v250, v246, v248
	v_mov_b32_e32 v251, v250
	s_waitcnt lgkmcnt(0)
	v_mfma_scale_f32_32x32x64_f8f6f4 v[4:19], v[232:239], v[224:231], v[4:19], v188, v188 op_sel_hi:[0,0,0]
	v_permlane32_swap_b32_e32 v250, v251
	v_max_f32_e32 v250, v250, v251
	v_sub_f32_e32 v155, v250, v154
	v_max_f32_e32 v153, v154, v250
	v_sub_f32_e32 v2, v154, v153
	v_mul_f32_e32 v2, 0x3e0293ee, v2
	v_exp_f32_e32 v2, v2
	v_cmp_ge_f32_e32 vcc, s55, v155
	s_cmp_eq_u64 vcc, exec
	s_cselect_b64 s[4:5], -1, 0
	s_barrier
	s_waitcnt vmcnt(2)
	v_cndmask_b32_e64 v2, v2, 1.0, s[4:5]
	s_waitcnt vmcnt(1)
	v_mov_b32_e32 v156, v124
	v_mov_b32_e32 v157, v126
	v_mov_b32_e32 v126, v125
	v_cmp_gt_f32_e32 vcc, 1.0, v2
	ds_write_b64 v189, v[156:157] offset:16384
	ds_write_b64 v190, v[126:127] offset:16384
	s_waitcnt vmcnt(0)
	ds_write_b128 v191, v[128:131] offset:49152
	s_cbranch_vccz .LBB0_419
	s_and_saveexec_b64 s[10:11], s[6:7]
	ds_write_b32 v184, v2 offset:128
	s_or_b64 exec, exec, s[10:11]
	s_waitcnt lgkmcnt(0)
	v_add_u32_e32 v155, v135, v185
	ds_read_b128 v[124:127], v155 offset:224
	ds_read_b128 v[128:131], v155 offset:192
	ds_read_b128 v[156:159], v155 offset:160
	ds_read_b128 v[166:169], v155 offset:128
	s_waitcnt lgkmcnt(3)
	v_pk_mul_f32 v[64:65], v[64:65], v[124:125]
	s_waitcnt lgkmcnt(2)
	v_pk_mul_f32 v[60:61], v[60:61], v[128:129]
	s_waitcnt lgkmcnt(1)
	v_pk_mul_f32 v[56:57], v[56:57], v[156:157]
	v_pk_mul_f32 v[66:67], v[66:67], v[126:127]
	v_pk_mul_f32 v[62:63], v[62:63], v[130:131]
	v_pk_mul_f32 v[58:59], v[58:59], v[158:159]
	s_waitcnt lgkmcnt(0)
	v_pk_mul_f32 v[54:55], v[54:55], v[168:169]
	v_pk_mul_f32 v[52:53], v[52:53], v[166:167]
	v_pk_mul_f32 v[48:49], v[48:49], v[124:125]
	v_pk_mul_f32 v[44:45], v[44:45], v[128:129]
	v_pk_mul_f32 v[40:41], v[40:41], v[156:157]
	v_pk_mul_f32 v[50:51], v[50:51], v[126:127]
	v_pk_mul_f32 v[46:47], v[46:47], v[130:131]
	v_pk_mul_f32 v[42:43], v[42:43], v[158:159]
	v_pk_mul_f32 v[38:39], v[38:39], v[168:169]
	v_pk_mul_f32 v[36:37], v[36:37], v[166:167]
	v_pk_mul_f32 v[32:33], v[32:33], v[124:125]
	v_pk_mul_f32 v[28:29], v[28:29], v[128:129]
	v_pk_mul_f32 v[24:25], v[24:25], v[156:157]
	v_pk_mul_f32 v[34:35], v[34:35], v[126:127]
	v_pk_mul_f32 v[30:31], v[30:31], v[130:131]
	v_pk_mul_f32 v[26:27], v[26:27], v[158:159]
	v_pk_mul_f32 v[22:23], v[22:23], v[168:169]
	v_pk_mul_f32 v[20:21], v[20:21], v[166:167]
	v_pk_mul_f32 v[16:17], v[16:17], v[124:125]
	v_pk_mul_f32 v[12:13], v[12:13], v[128:129]
	v_pk_mul_f32 v[8:9], v[8:9], v[156:157]
	v_pk_mul_f32 v[18:19], v[18:19], v[126:127]
	v_pk_mul_f32 v[14:15], v[14:15], v[130:131]
	v_pk_mul_f32 v[10:11], v[10:11], v[158:159]
	v_pk_mul_f32 v[6:7], v[6:7], v[168:169]
	v_pk_mul_f32 v[4:5], v[4:5], v[166:167]

	.amdhsa_kernel _Z10fwd_kernel4Args
		.amdhsa_group_segment_fixed_size 0
		.amdhsa_private_segment_fixed_size 0
		.amdhsa_kernarg_size 456
		.amdhsa_user_sgpr_count 2
		.amdhsa_user_sgpr_dispatch_ptr 0
		.amdhsa_user_sgpr_queue_ptr 0
		.amdhsa_user_sgpr_kernarg_segment_ptr 1
		.amdhsa_user_sgpr_dispatch_id 0
		.amdhsa_user_sgpr_kernarg_preload_length 0
		.amdhsa_user_sgpr_kernarg_preload_offset 0
		.amdhsa_user_sgpr_private_segment_size 0
		.amdhsa_uses_dynamic_stack 0
		.amdhsa_enable_private_segment 0
		.amdhsa_system_sgpr_workgroup_id_x 1
		.amdhsa_system_sgpr_workgroup_id_y 0
		.amdhsa_system_sgpr_workgroup_id_z 0
		.amdhsa_system_sgpr_workgroup_info 0
		.amdhsa_system_vgpr_workitem_id 0
		.amdhsa_next_free_vgpr 256
		.amdhsa_next_free_sgpr 98
		.amdhsa_accum_offset 256
		.amdhsa_reserve_vcc 1
		.amdhsa_float_round_mode_32 0
		.amdhsa_float_round_mode_16_64 0
		.amdhsa_float_denorm_mode_32 3
		.amdhsa_float_denorm_mode_16_64 3
		.amdhsa_dx10_clamp 1
		.amdhsa_ieee_mode 1
		.amdhsa_fp16_overflow 0
		.amdhsa_tg_split 0
		.amdhsa_exception_fp_ieee_invalid_op 0
		.amdhsa_exception_fp_denorm_src 0
		.amdhsa_exception_fp_ieee_div_zero 0
		.amdhsa_exception_fp_ieee_overflow 0
		.amdhsa_exception_fp_ieee_underflow 0
		.amdhsa_exception_fp_ieee_inexact 0
		.amdhsa_exception_int_div_zero 0
	.end_amdhsa_kernel

amdhsa.kernels:
  - .agpr_count:     0
    .args:
      - .offset:         0
        .size:           200
        .value_kind:     by_value
      - .offset:         200
        .size:           4
        .value_kind:     hidden_block_count_x
      - .offset:         204
        .size:           4
        .value_kind:     hidden_block_count_y
      - .offset:         208
        .size:           4
        .value_kind:     hidden_block_count_z
      - .offset:         212
        .size:           2
        .value_kind:     hidden_group_size_x
      - .offset:         214
        .size:           2
        .value_kind:     hidden_group_size_y
      - .offset:         216
        .size:           2
        .value_kind:     hidden_group_size_z
      - .offset:         218
        .size:           2
        .value_kind:     hidden_remainder_x
      - .offset:         220
        .size:           2
        .value_kind:     hidden_remainder_y
      - .offset:         222
        .size:           2
        .value_kind:     hidden_remainder_z
      - .offset:         240
        .size:           8
        .value_kind:     hidden_global_offset_x
      - .offset:         248
        .size:           8
        .value_kind:     hidden_global_offset_y
      - .offset:         256
        .size:           8
        .value_kind:     hidden_global_offset_z
      - .offset:         264
        .size:           2
        .value_kind:     hidden_grid_dims
      - .offset:         320
        .size:           4
        .value_kind:     hidden_dynamic_lds_size
    .group_segment_fixed_size: 0
    .kernarg_segment_align: 8
    .kernarg_segment_size: 456
    .language:       OpenCL C
    .language_version:
      - 2
      - 0
    .max_flat_workgroup_size: 512
    .name:           _Z10fwd_kernel4Args
    .private_segment_fixed_size: 0
    .sgpr_count:     104
    .sgpr_spill_count: 97
    .symbol:         _Z10fwd_kernel4Args.kd
    .uniform_work_group_size: 1
    .uses_dynamic_stack: false
    .vgpr_count:     256
    .vgpr_spill_count: 0
    .wavefront_size: 64
